# gcn2 front: mask coefficients in f32 then v_cvt_pk_f16_f32 (replaces 4 cvt + 2 pack per block)
# baseline (speedup 1.0000x reference)
.Lg2f_b0_gen:
	v_add_u32_e32 v112, s29, v86
	v_add_u32_e32 v113, s29, v89
	v_min_i32_e32 v112, v112, v110
	v_lshl_add_u32 v114, v113, 3, v104
	v_lshl_add_u32 v112, v112, 3, v104
	ds_read2_b32 v[116:117], v114 offset0:1 offset1:3
	ds_read2_b32 v[118:119], v114 offset0:5 offset1:7
	ds_read_b32 v68, v112
	v_sub_u32_e32 v113, v113, v101
	v_add_u32_e32 v114, 1, v113
	v_add_u32_e32 v115, 2, v113
	v_add_u32_e32 v120, 3, v113
	v_cmp_gt_u32_e64 s[42:43], v102, v113
	v_cmp_gt_u32_e64 s[44:45], v102, v114
	v_cmp_gt_u32_e64 s[46:47], v102, v115
	v_cmp_gt_u32_e64 s[48:49], v102, v120
	s_waitcnt lgkmcnt(1)
	v_cndmask_b32_e64 v116, 0, v116, s[42:43]
	v_cndmask_b32_e64 v117, 0, v117, s[44:45]
	v_cndmask_b32_e64 v118, 0, v118, s[46:47]
	v_cndmask_b32_e64 v119, 0, v119, s[48:49]
	v_cvt_pk_f16_f32 v66, v116, v117
	v_cvt_pk_f16_f32 v67, v118, v119
	s_waitcnt lgkmcnt(0)

.Lg2f_b1_gen:
	s_add_i32 s41, s29, 16
	v_add_u32_e32 v112, s41, v86
	v_add_u32_e32 v113, s41, v89
	v_min_i32_e32 v112, v112, v110
	v_lshl_add_u32 v114, v113, 3, v104
	v_lshl_add_u32 v112, v112, 3, v104
	ds_read2_b32 v[116:117], v114 offset0:1 offset1:3
	ds_read2_b32 v[118:119], v114 offset0:5 offset1:7
	ds_read_b32 v74, v112
	v_sub_u32_e32 v113, v113, v101
	v_add_u32_e32 v114, 1, v113
	v_add_u32_e32 v115, 2, v113
	v_add_u32_e32 v120, 3, v113
	v_cmp_gt_u32_e64 s[42:43], v102, v113
	v_cmp_gt_u32_e64 s[44:45], v102, v114
	v_cmp_gt_u32_e64 s[46:47], v102, v115
	v_cmp_gt_u32_e64 s[48:49], v102, v120
	s_waitcnt lgkmcnt(1)
	v_cndmask_b32_e64 v116, 0, v116, s[42:43]
	v_cndmask_b32_e64 v117, 0, v117, s[44:45]
	v_cndmask_b32_e64 v118, 0, v118, s[46:47]
	v_cndmask_b32_e64 v119, 0, v119, s[48:49]
	v_cvt_pk_f16_f32 v68, v116, v117
	v_cvt_pk_f16_f32 v69, v118, v119
	s_waitcnt lgkmcnt(0)
